# inproj GEMM: next tile's first two k-tiles (A and B rows) touched into L2 before the last two k-tiles of the current tile
# baseline (speedup 1.0000x reference)
; DI int gemm_rb(int m0) { const int t = ftid(); return m0 + ((t >> 8) & 1) * 64 + (t & 15); }
; DI int gemm_cb(int n0) { const int t = ftid(); return n0 + ((t >> 6) & 3) * 32 + 8 * ((t >> 4) & 3); }
; #define STA(b, h, kt) do { _Pragma("unroll") for (int i_ = 0; i_ < 2; ++i_) __builtin_amdgcn_global_load_lds((const unsigned*)(((kt) < ks ? ab : ab2) + (h) * ah + (kt) * 64 + aoff[i_]), (LAS unsigned*)(lds + ((b) * 2 + (h)) * 16384 + wid * 1024 + i_ * 8192), 16, 0, 0); } while (0)
; #define STB(b, h, kt) do { _Pragma("unroll") for (int i_ = 0; i_ < 2; ++i_) __builtin_amdgcn_global_load_lds((const unsigned*)(((kt) < ks ? bb : bb2) + (h) * bh + (kt) * 64 + boff[i_]), (LAS unsigned*)(lds + 65536 + ((b) * 2 + (h)) * 16384 + wid * 1024 + i_ * 8192), 16, 0, 0); } while (0)
; #define LDA_(dst, b, h) do { _Pragma("unroll") for (int m_ = 0; m_ < 4; ++m_) _Pragma("unroll") for (int k_ = 0; k_ < 2; ++k_) dst[m_][k_] = *(const bf16x8*)(la + ((b) * 2 + (h)) * 16384 + (m_ * 2 + k_) * 1024); } while (0)
; #define LDB_(dst, b, h) do { _Pragma("unroll") for (int n_ = 0; n_ < 2; ++n_) _Pragma("unroll") for (int k_ = 0; k_ < 2; ++k_) dst[n_][k_] = *(const bf16x8*)(lb + ((b) * 2 + (h)) * 16384 + (n_ * 2 + k_) * 1024); } while (0)
; #define WAIT_V(n) asm volatile("s_waitcnt vmcnt(" #n ")" ::: "memory")
; #define WAIT_L(n) asm volatile("s_waitcnt lgkmcnt(" #n ")" ::: "memory")
; #define BAR __builtin_amdgcn_s_barrier()
; template <bool ZERO, class Mid>
; DI void gemm_core(const GemmArgs& g, int m0, int n0, char* lds, f32x4 (&acc)[8][4], const Mid& mid) {
;     ...
;   for (int t = 0; t < nt - 2; t += 2) {
;     if (t == ks) { mid.apply(acc, gemm_rb(m0), gemm_cb(n0)); SCHED; }
;     LDB_(B0, 0, 0); SCHED; LDA_(At, 0, 0); STA(1, 1, t + 1);
;     WAIT_L(8); BAR; WAIT_L(0); MMA_(0, 0, B0); BAR; SCHED;
;     LDB_(B1, 0, 1); STB(0, 0, t + 2);
;     BAR; WAIT_L(0); MMA_(0, 1, B1); BAR;
;     LDA_(At, 0, 1); STA(0, 0, t + 2);
;     BAR; WAIT_L(0); MMA_(1, 0, B0); BAR; SCHED;
;     STB(0, 1, t + 2);
;     WAIT_V(6); BAR; MMA_(1, 1, B1); BAR;
;     LDB_(B0, 1, 0); SCHED; LDA_(At, 1, 0); STA(0, 1, t + 2);
;     WAIT_L(8); BAR; WAIT_L(0); MMA_(0, 0, B0); BAR; SCHED;
;     LDB_(B1, 1, 1); STB(1, 0, t + 3);
;     BAR; WAIT_L(0); MMA_(0, 1, B1); BAR;
;     LDA_(At, 1, 1); STA(1, 0, t + 3);
;     BAR; WAIT_L(0); MMA_(1, 0, B0); BAR; SCHED;
;     STB(1, 1, t + 3);
;     WAIT_V(6); BAR; MMA_(1, 1, B1); BAR;
.LBB0_233:
	ds_read_b128 v[164:167], v143
	ds_read_b128 v[168:171], v143 offset:1024
	ds_read_b128 v[172:175], v143 offset:2048
	ds_read_b128 v[178:181], v143 offset:3072
	v_add_u32_e32 v161, 0xc000, v149
	v_lshl_add_u64 v[186:187], s[8:9], 0, v[136:137]
	v_readfirstlane_b32 s5, v161
	v_lshl_add_u64 v[162:163], v[186:187], 0, s[28:29]
	s_mov_b32 m0, s5
	ds_read_b128 v[182:185], v141
	ds_read_b128 v[196:199], v141 offset:1024
	ds_read_b128 v[200:203], v141 offset:2048
	ds_read_b128 v[208:211], v141 offset:3072
	ds_read_b128 v[212:215], v141 offset:4096
	ds_read_b128 v[216:219], v141 offset:5120
	ds_read_b128 v[220:223], v141 offset:6144
	ds_read_b128 v[224:227], v141 offset:7168
	global_load_lds_dwordx4 v[162:163], off
	v_add_u32_e32 v162, 0xe000, v149
	v_lshl_add_u64 v[204:205], s[8:9], 0, v[138:139]
	v_readfirstlane_b32 s5, v162
	v_lshl_add_u64 v[228:229], v[204:205], 0, s[28:29]
	s_mov_b32 m0, s5
	s_nop 0
	global_load_lds_dwordx4 v[228:229], off
	s_waitcnt lgkmcnt(8)
	s_barrier
	s_waitcnt lgkmcnt(0)
	s_setprio 1
	s_waitcnt lgkmcnt(0)
	v_mfma_f32_16x16x32_bf16 v[124:127], v[164:167], v[182:185], v[124:127]
	v_mfma_f32_16x16x32_bf16 v[120:123], v[172:175], v[182:185], v[120:123]
	v_mfma_f32_16x16x32_bf16 v[116:119], v[164:167], v[200:203], v[116:119]
	v_mfma_f32_16x16x32_bf16 v[112:115], v[172:175], v[200:203], v[112:115]
	v_mfma_f32_16x16x32_bf16 v[104:107], v[164:167], v[212:215], v[104:107]
	v_mfma_f32_16x16x32_bf16 v[96:99], v[172:175], v[212:215], v[96:99]
	v_mfma_f32_16x16x32_bf16 v[88:91], v[164:167], v[220:223], v[88:91]
	v_mfma_f32_16x16x32_bf16 v[80:83], v[172:175], v[220:223], v[80:83]
	v_mfma_f32_16x16x32_bf16 v[124:127], v[168:171], v[196:199], v[124:127]
	v_mfma_f32_16x16x32_bf16 v[120:123], v[178:181], v[196:199], v[120:123]
	v_mfma_f32_16x16x32_bf16 v[116:119], v[168:171], v[208:211], v[116:119]
	v_mfma_f32_16x16x32_bf16 v[112:115], v[178:181], v[208:211], v[112:115]
	v_mfma_f32_16x16x32_bf16 v[104:107], v[168:171], v[216:219], v[104:107]
	v_mfma_f32_16x16x32_bf16 v[96:99], v[178:181], v[216:219], v[96:99]
	v_mfma_f32_16x16x32_bf16 v[88:91], v[168:171], v[224:227], v[88:91]
	v_mfma_f32_16x16x32_bf16 v[80:83], v[178:181], v[224:227], v[80:83]
	s_setprio 0
	s_barrier
	v_lshl_add_u64 v[244:245], s[8:9], 0, v[132:133]
	v_readfirstlane_b32 s5, v142
	v_lshl_add_u64 v[246:247], v[244:245], 0, s[30:31]
	s_mov_b32 m0, s5
	ds_read_b128 v[228:231], v143 offset:16384
	ds_read_b128 v[232:235], v143 offset:17408
	ds_read_b128 v[236:239], v143 offset:18432
	ds_read_b128 v[240:243], v143 offset:19456
	global_load_lds_dwordx4 v[246:247], off
	v_lshl_add_u64 v[246:247], s[8:9], 0, v[134:135]
	v_readfirstlane_b32 s5, v144
	v_lshl_add_u64 v[248:249], v[246:247], 0, s[30:31]
	s_mov_b32 m0, s5
	s_nop 0
	global_load_lds_dwordx4 v[248:249], off
	s_barrier
	s_waitcnt lgkmcnt(0)
	s_setprio 1
	s_waitcnt lgkmcnt(0)
	v_mfma_f32_16x16x32_bf16 v[108:111], v[228:231], v[182:185], v[108:111]
	v_mfma_f32_16x16x32_bf16 v[100:103], v[236:239], v[182:185], v[100:103]
	v_mfma_f32_16x16x32_bf16 v[92:95], v[228:231], v[200:203], v[92:95]
	v_mfma_f32_16x16x32_bf16 v[84:87], v[236:239], v[200:203], v[84:87]
	v_mfma_f32_16x16x32_bf16 v[76:79], v[228:231], v[212:215], v[76:79]
	v_mfma_f32_16x16x32_bf16 v[72:75], v[236:239], v[212:215], v[72:75]
	v_mfma_f32_16x16x32_bf16 v[64:67], v[228:231], v[220:223], v[64:67]
	v_mfma_f32_16x16x32_bf16 v[60:63], v[236:239], v[220:223], v[60:63]
	v_mfma_f32_16x16x32_bf16 v[108:111], v[232:235], v[196:199], v[108:111]
	v_mfma_f32_16x16x32_bf16 v[100:103], v[240:243], v[196:199], v[100:103]
	v_mfma_f32_16x16x32_bf16 v[92:95], v[232:235], v[208:211], v[92:95]
	v_mfma_f32_16x16x32_bf16 v[84:87], v[240:243], v[208:211], v[84:87]
	v_mfma_f32_16x16x32_bf16 v[76:79], v[232:235], v[216:219], v[76:79]
	v_mfma_f32_16x16x32_bf16 v[72:75], v[240:243], v[216:219], v[72:75]
	v_mfma_f32_16x16x32_bf16 v[64:67], v[232:235], v[224:227], v[64:67]
	v_mfma_f32_16x16x32_bf16 v[60:63], v[240:243], v[224:227], v[60:63]
	s_setprio 0
	v_readfirstlane_b32 s5, v149
	v_lshl_add_u64 v[248:249], v[186:187], 0, s[34:35]
	s_mov_b32 m0, s5
	v_readfirstlane_b32 s5, v150
	s_barrier
	ds_read_b128 v[182:185], v141 offset:16384
	ds_read_b128 v[196:199], v141 offset:17408
	ds_read_b128 v[200:203], v141 offset:18432
	ds_read_b128 v[208:211], v141 offset:19456
	ds_read_b128 v[212:215], v141 offset:20480
	ds_read_b128 v[216:219], v141 offset:21504
	ds_read_b128 v[220:223], v141 offset:22528
	ds_read_b128 v[224:227], v141 offset:23552
	global_load_lds_dwordx4 v[248:249], off
	v_lshl_add_u64 v[248:249], v[204:205], 0, s[34:35]
	s_mov_b32 m0, s5
	s_nop 0
	global_load_lds_dwordx4 v[248:249], off
	s_barrier
	s_waitcnt lgkmcnt(0)
	s_setprio 1
	s_waitcnt lgkmcnt(0)
	v_mfma_f32_16x16x32_bf16 v[56:59], v[164:167], v[182:185], v[56:59]
	v_mfma_f32_16x16x32_bf16 v[52:55], v[172:175], v[182:185], v[52:55]
	v_mfma_f32_16x16x32_bf16 v[48:51], v[164:167], v[200:203], v[48:51]
	v_mfma_f32_16x16x32_bf16 v[40:43], v[172:175], v[200:203], v[40:43]
	v_mfma_f32_16x16x32_bf16 v[32:35], v[164:167], v[212:215], v[32:35]
	v_mfma_f32_16x16x32_bf16 v[24:27], v[172:175], v[212:215], v[24:27]
	v_mfma_f32_16x16x32_bf16 v[16:19], v[164:167], v[220:223], v[16:19]
	v_mfma_f32_16x16x32_bf16 v[8:11], v[172:175], v[220:223], v[8:11]
	v_mfma_f32_16x16x32_bf16 v[56:59], v[168:171], v[196:199], v[56:59]
	v_mfma_f32_16x16x32_bf16 v[52:55], v[178:181], v[196:199], v[52:55]
	v_mfma_f32_16x16x32_bf16 v[48:51], v[168:171], v[208:211], v[48:51]
	v_mfma_f32_16x16x32_bf16 v[40:43], v[178:181], v[208:211], v[40:43]
	v_mfma_f32_16x16x32_bf16 v[32:35], v[168:171], v[216:219], v[32:35]
	v_mfma_f32_16x16x32_bf16 v[24:27], v[178:181], v[216:219], v[24:27]
	v_mfma_f32_16x16x32_bf16 v[16:19], v[168:171], v[224:227], v[16:19]
	v_mfma_f32_16x16x32_bf16 v[8:11], v[178:181], v[224:227], v[8:11]
	s_setprio 0
	s_barrier
; DI int gemm_rb(int m0) { const int t = ftid(); return m0 + ((t >> 8) & 1) * 64 + (t & 15); }
; DI int gemm_cb(int n0) { const int t = ftid(); return n0 + ((t >> 6) & 3) * 32 + 8 * ((t >> 4) & 3); }
; #define STA(b, h, kt) do { _Pragma("unroll") for (int i_ = 0; i_ < 2; ++i_) __builtin_amdgcn_global_load_lds((const unsigned*)(((kt) < ks ? ab : ab2) + (h) * ah + (kt) * 64 + aoff[i_]), (LAS unsigned*)(lds + ((b) * 2 + (h)) * 16384 + wid * 1024 + i_ * 8192), 16, 0, 0); } while (0)
; #define STB(b, h, kt) do { _Pragma("unroll") for (int i_ = 0; i_ < 2; ++i_) __builtin_amdgcn_global_load_lds((const unsigned*)(((kt) < ks ? bb : bb2) + (h) * bh + (kt) * 64 + boff[i_]), (LAS unsigned*)(lds + 65536 + ((b) * 2 + (h)) * 16384 + wid * 1024 + i_ * 8192), 16, 0, 0); } while (0)
; #define LDA_(dst, b, h) do { _Pragma("unroll") for (int m_ = 0; m_ < 4; ++m_) _Pragma("unroll") for (int k_ = 0; k_ < 2; ++k_) dst[m_][k_] = *(const bf16x8*)(la + ((b) * 2 + (h)) * 16384 + (m_ * 2 + k_) * 1024); } while (0)
; #define LDB_(dst, b, h) do { _Pragma("unroll") for (int n_ = 0; n_ < 2; ++n_) _Pragma("unroll") for (int k_ = 0; k_ < 2; ++k_) dst[n_][k_] = *(const bf16x8*)(lb + ((b) * 2 + (h)) * 16384 + (n_ * 2 + k_) * 1024); } while (0)
; #define WAIT_V(n) asm volatile("s_waitcnt vmcnt(" #n ")" ::: "memory")
; #define WAIT_L(n) asm volatile("s_waitcnt lgkmcnt(" #n ")" ::: "memory")
; #define BAR __builtin_amdgcn_s_barrier()
; template <bool ZERO, class Mid>
; DI void gemm_core(const GemmArgs& g, int m0, int n0, char* lds, f32x4 (&acc)[8][4], const Mid& mid) {
;     ...
;   for (int t = 0; t < nt - 2; t += 2) {
;     if (t == ks) { mid.apply(acc, gemm_rb(m0), gemm_cb(n0)); SCHED; }
;     LDB_(B0, 0, 0); SCHED; LDA_(At, 0, 0); STA(1, 1, t + 1);
;     WAIT_L(8); BAR; WAIT_L(0); MMA_(0, 0, B0); BAR; SCHED;
;     LDB_(B1, 0, 1); STB(0, 0, t + 2);
;     BAR; WAIT_L(0); MMA_(0, 1, B1); BAR;
;     LDA_(At, 0, 1); STA(0, 0, t + 2);
;     BAR; WAIT_L(0); MMA_(1, 0, B0); BAR; SCHED;
;     STB(0, 1, t + 2);
;     WAIT_V(6); BAR; MMA_(1, 1, B1); BAR;
;     LDB_(B0, 1, 0); SCHED; LDA_(At, 1, 0); STA(0, 1, t + 2);
;     WAIT_L(8); BAR; WAIT_L(0); MMA_(0, 0, B0); BAR; SCHED;
;     LDB_(B1, 1, 1); STB(1, 0, t + 3);
;     BAR; WAIT_L(0); MMA_(0, 1, B1); BAR;
;     LDA_(At, 1, 1); STA(1, 0, t + 3);
;     BAR; WAIT_L(0); MMA_(1, 0, B0); BAR; SCHED;
;     STB(1, 1, t + 3);
;     WAIT_V(6); BAR; MMA_(1, 1, B1); BAR;
	v_readfirstlane_b32 s5, v151
	v_lshl_add_u64 v[164:165], v[244:245], 0, s[38:39]
	s_mov_b32 m0, s5
	v_readfirstlane_b32 s5, v152
	global_load_lds_dwordx4 v[164:165], off
	v_lshl_add_u64 v[164:165], v[246:247], 0, s[38:39]
	s_mov_b32 m0, s5
	s_nop 0
	global_load_lds_dwordx4 v[164:165], off
	s_waitcnt vmcnt(6)
	s_barrier
	s_setprio 1
	v_mfma_f32_16x16x32_bf16 v[44:47], v[228:231], v[182:185], v[44:47]
	v_mfma_f32_16x16x32_bf16 v[36:39], v[236:239], v[182:185], v[36:39]
	v_mfma_f32_16x16x32_bf16 v[28:31], v[228:231], v[200:203], v[28:31]
	v_mfma_f32_16x16x32_bf16 v[20:23], v[236:239], v[200:203], v[20:23]
	v_mfma_f32_16x16x32_bf16 v[12:15], v[228:231], v[212:215], v[12:15]
	v_mfma_f32_16x16x32_bf16 v[4:7], v[236:239], v[212:215], v[4:7]
	v_mfma_f32_16x16x32_bf16 v[0:3], v[228:231], v[220:223], v[0:3]
	v_mfma_f32_16x16x32_bf16 v[68:71], v[236:239], v[220:223], v[68:71]
	v_mfma_f32_16x16x32_bf16 v[44:47], v[232:235], v[196:199], v[44:47]
	v_mfma_f32_16x16x32_bf16 v[36:39], v[240:243], v[196:199], v[36:39]
	v_mfma_f32_16x16x32_bf16 v[28:31], v[232:235], v[208:211], v[28:31]
	v_mfma_f32_16x16x32_bf16 v[20:23], v[240:243], v[208:211], v[20:23]
	v_mfma_f32_16x16x32_bf16 v[12:15], v[232:235], v[216:219], v[12:15]
	v_mfma_f32_16x16x32_bf16 v[4:7], v[240:243], v[216:219], v[4:7]
	v_mfma_f32_16x16x32_bf16 v[0:3], v[232:235], v[224:227], v[0:3]
	v_mfma_f32_16x16x32_bf16 v[68:71], v[240:243], v[224:227], v[68:71]
	s_setprio 0
	s_barrier
	ds_read_b128 v[164:167], v143 offset:32768
	ds_read_b128 v[168:171], v143 offset:33792
	ds_read_b128 v[172:175], v143 offset:34816
	ds_read_b128 v[178:181], v143 offset:35840
	v_readfirstlane_b32 s5, v153
	v_lshl_add_u64 v[228:229], v[186:187], 0, s[40:41]
	s_mov_b32 m0, s5
	v_readfirstlane_b32 s5, v154
	ds_read_b128 v[182:185], v141 offset:32768
	ds_read_b128 v[196:199], v141 offset:33792
	ds_read_b128 v[200:203], v141 offset:34816
	ds_read_b128 v[208:211], v141 offset:35840
	ds_read_b128 v[212:215], v141 offset:36864
	ds_read_b128 v[216:219], v141 offset:37888
	ds_read_b128 v[220:223], v141 offset:38912
	ds_read_b128 v[224:227], v141 offset:39936
	global_load_lds_dwordx4 v[228:229], off
	v_lshl_add_u64 v[228:229], v[204:205], 0, s[40:41]
	s_mov_b32 m0, s5
	s_nop 0
	global_load_lds_dwordx4 v[228:229], off
	s_waitcnt lgkmcnt(8)
	s_barrier
	s_waitcnt lgkmcnt(0)
	s_setprio 1
	s_waitcnt lgkmcnt(0)
	v_mfma_f32_16x16x32_bf16 v[124:127], v[164:167], v[182:185], v[124:127]
	v_mfma_f32_16x16x32_bf16 v[120:123], v[172:175], v[182:185], v[120:123]
	v_mfma_f32_16x16x32_bf16 v[116:119], v[164:167], v[200:203], v[116:119]
	v_mfma_f32_16x16x32_bf16 v[112:115], v[172:175], v[200:203], v[112:115]
	v_mfma_f32_16x16x32_bf16 v[104:107], v[164:167], v[212:215], v[104:107]
	v_mfma_f32_16x16x32_bf16 v[96:99], v[172:175], v[212:215], v[96:99]
	v_mfma_f32_16x16x32_bf16 v[88:91], v[164:167], v[220:223], v[88:91]
	v_mfma_f32_16x16x32_bf16 v[80:83], v[172:175], v[220:223], v[80:83]
	v_mfma_f32_16x16x32_bf16 v[124:127], v[168:171], v[196:199], v[124:127]
	v_mfma_f32_16x16x32_bf16 v[120:123], v[178:181], v[196:199], v[120:123]
	v_mfma_f32_16x16x32_bf16 v[116:119], v[168:171], v[208:211], v[116:119]
	v_mfma_f32_16x16x32_bf16 v[112:115], v[178:181], v[208:211], v[112:115]
	v_mfma_f32_16x16x32_bf16 v[104:107], v[168:171], v[216:219], v[104:107]
	v_mfma_f32_16x16x32_bf16 v[96:99], v[178:181], v[216:219], v[96:99]
	v_mfma_f32_16x16x32_bf16 v[88:91], v[168:171], v[224:227], v[88:91]
	v_mfma_f32_16x16x32_bf16 v[80:83], v[178:181], v[224:227], v[80:83]
	s_setprio 0
	s_barrier
	v_readfirstlane_b32 s5, v155
	v_lshl_add_u64 v[248:249], v[244:245], 0, s[42:43]
	s_mov_b32 m0, s5
	v_readfirstlane_b32 s5, v156
	ds_read_b128 v[228:231], v143 offset:49152
	ds_read_b128 v[232:235], v143 offset:50176
	ds_read_b128 v[236:239], v143 offset:51200
	ds_read_b128 v[240:243], v143 offset:52224
	global_load_lds_dwordx4 v[248:249], off
	v_lshl_add_u64 v[248:249], v[246:247], 0, s[42:43]
	s_mov_b32 m0, s5
	s_nop 0
	global_load_lds_dwordx4 v[248:249], off
	s_barrier
	s_waitcnt lgkmcnt(0)
	s_setprio 1
	s_waitcnt lgkmcnt(0)
	v_mfma_f32_16x16x32_bf16 v[108:111], v[228:231], v[182:185], v[108:111]
	v_mfma_f32_16x16x32_bf16 v[100:103], v[236:239], v[182:185], v[100:103]
	v_mfma_f32_16x16x32_bf16 v[92:95], v[228:231], v[200:203], v[92:95]
	v_mfma_f32_16x16x32_bf16 v[84:87], v[236:239], v[200:203], v[84:87]
	v_mfma_f32_16x16x32_bf16 v[76:79], v[228:231], v[212:215], v[76:79]
	v_mfma_f32_16x16x32_bf16 v[72:75], v[236:239], v[212:215], v[72:75]
	v_mfma_f32_16x16x32_bf16 v[64:67], v[228:231], v[220:223], v[64:67]
	v_mfma_f32_16x16x32_bf16 v[60:63], v[236:239], v[220:223], v[60:63]
	v_mfma_f32_16x16x32_bf16 v[108:111], v[232:235], v[196:199], v[108:111]
	v_mfma_f32_16x16x32_bf16 v[100:103], v[240:243], v[196:199], v[100:103]
	v_mfma_f32_16x16x32_bf16 v[92:95], v[232:235], v[208:211], v[92:95]
	v_mfma_f32_16x16x32_bf16 v[84:87], v[240:243], v[208:211], v[84:87]
	v_mfma_f32_16x16x32_bf16 v[76:79], v[232:235], v[216:219], v[76:79]
	v_mfma_f32_16x16x32_bf16 v[72:75], v[240:243], v[216:219], v[72:75]
	v_mfma_f32_16x16x32_bf16 v[64:67], v[232:235], v[224:227], v[64:67]
	v_mfma_f32_16x16x32_bf16 v[60:63], v[240:243], v[224:227], v[60:63]
	s_setprio 0
	v_readfirstlane_b32 s5, v157
	v_lshl_add_u64 v[186:187], v[186:187], 0, s[44:45]
	s_mov_b32 m0, s5
	v_readfirstlane_b32 s5, v158
	s_barrier
	ds_read_b128 v[182:185], v141 offset:49152
	ds_read_b128 v[196:199], v141 offset:50176
	ds_read_b128 v[200:203], v141 offset:51200
	ds_read_b128 v[208:211], v141 offset:52224
	ds_read_b128 v[212:215], v141 offset:53248
	ds_read_b128 v[216:219], v141 offset:54272
	ds_read_b128 v[220:223], v141 offset:55296
	ds_read_b128 v[224:227], v141 offset:56320
	global_load_lds_dwordx4 v[186:187], off
	v_lshl_add_u64 v[186:187], v[204:205], 0, s[44:45]
	s_mov_b32 m0, s5
	s_nop 0
	global_load_lds_dwordx4 v[186:187], off
	s_barrier
; #define STA(b, h, kt) do { _Pragma("unroll") for (int i_ = 0; i_ < 2; ++i_) __builtin_amdgcn_global_load_lds((const unsigned*)(((kt) < ks ? ab : ab2) + (h) * ah + (kt) * 64 + aoff[i_]), (LAS unsigned*)(lds + ((b) * 2 + (h)) * 16384 + wid * 1024 + i_ * 8192), 16, 0, 0); } while (0)
; #define STB(b, h, kt) do { _Pragma("unroll") for (int i_ = 0; i_ < 2; ++i_) __builtin_amdgcn_global_load_lds((const unsigned*)(((kt) < ks ? bb : bb2) + (h) * bh + (kt) * 64 + boff[i_]), (LAS unsigned*)(lds + 65536 + ((b) * 2 + (h)) * 16384 + wid * 1024 + i_ * 8192), 16, 0, 0); } while (0)
; #define LDA_(dst, b, h) do { _Pragma("unroll") for (int m_ = 0; m_ < 4; ++m_) _Pragma("unroll") for (int k_ = 0; k_ < 2; ++k_) dst[m_][k_] = *(const bf16x8*)(la + ((b) * 2 + (h)) * 16384 + (m_ * 2 + k_) * 1024); } while (0)
; #define LDB_(dst, b, h) do { _Pragma("unroll") for (int n_ = 0; n_ < 2; ++n_) _Pragma("unroll") for (int k_ = 0; k_ < 2; ++k_) dst[n_][k_] = *(const bf16x8*)(lb + ((b) * 2 + (h)) * 16384 + (n_ * 2 + k_) * 1024); } while (0)
; #define MMA_(ai, bj, Bx) do { __builtin_amdgcn_s_setprio(1); _Pragma("unroll") for (int m_ = 0; m_ < 4; ++m_) _Pragma("unroll") for (int n_ = 0; n_ < 2; ++n_) _Pragma("unroll") for (int k_ = 0; k_ < 2; ++k_) \
;     acc[(ai) * 4 + m_][(bj) * 2 + n_] = MFMA16(Bx[n_][k_], At[m_][k_], acc[(ai) * 4 + m_][(bj) * 2 + n_]); __builtin_amdgcn_s_setprio(0); } while (0)
; #define WAIT_V(n) asm volatile("s_waitcnt vmcnt(" #n ")" ::: "memory")
; #define WAIT_L(n) asm volatile("s_waitcnt lgkmcnt(" #n ")" ::: "memory")
; #define BAR __builtin_amdgcn_s_barrier()
; #define SCHED __builtin_amdgcn_sched_barrier(0)
; template <bool ZERO, class Mid>
; DI void gemm_core(const GemmArgs& g, int m0, int n0, char* lds, f32x4 (&acc)[8][4], const Mid& mid) {
;     ...
;     LDA_(At, 1, 1); STA(1, 0, t + 3);
;     BAR; WAIT_L(0); MMA_(1, 0, B0); BAR; SCHED;
;     STB(1, 1, t + 3);
;     WAIT_V(6); BAR; MMA_(1, 1, B1); BAR;
;   }
;   { LDB_(B0, 0, 0); LDA_(At, 0, 0); STA(1, 1, nt - 1);
;   DI bool next(int& m, int& n) {
;     if (L >= total) return false;
;     if (L < 64 * nfull) { const int ng = L >> 6, rem = L & 63, mg = rem >> 5, ni = (rem & 31) >> 3, mi = rem & 7; m = 16 * x + 8 * mg + mi; n = 4 * ng + ((ni + 2 * mg) & 3); }
;     else { const int Lp = L - 64 * nfull; m = 16 * x + (Lp & 15); n = 4 * nfull + (Lp >> 4); }
;     L += R;
;     return true;
	s_waitcnt lgkmcnt(0)
	s_setprio 1
	s_waitcnt lgkmcnt(0)
	v_mfma_f32_16x16x32_bf16 v[56:59], v[164:167], v[182:185], v[56:59]
	v_mfma_f32_16x16x32_bf16 v[52:55], v[172:175], v[182:185], v[52:55]
	v_mfma_f32_16x16x32_bf16 v[48:51], v[164:167], v[200:203], v[48:51]
	v_mfma_f32_16x16x32_bf16 v[40:43], v[172:175], v[200:203], v[40:43]
	v_mfma_f32_16x16x32_bf16 v[32:35], v[164:167], v[212:215], v[32:35]
	v_mfma_f32_16x16x32_bf16 v[24:27], v[172:175], v[212:215], v[24:27]
	v_mfma_f32_16x16x32_bf16 v[16:19], v[164:167], v[220:223], v[16:19]
	v_mfma_f32_16x16x32_bf16 v[8:11], v[172:175], v[220:223], v[8:11]
	v_mfma_f32_16x16x32_bf16 v[56:59], v[168:171], v[196:199], v[56:59]
	v_mfma_f32_16x16x32_bf16 v[52:55], v[178:181], v[196:199], v[52:55]
	v_mfma_f32_16x16x32_bf16 v[48:51], v[168:171], v[208:211], v[48:51]
	v_mfma_f32_16x16x32_bf16 v[40:43], v[178:181], v[208:211], v[40:43]
	v_mfma_f32_16x16x32_bf16 v[32:35], v[168:171], v[216:219], v[32:35]
	v_mfma_f32_16x16x32_bf16 v[24:27], v[178:181], v[216:219], v[24:27]
	v_mfma_f32_16x16x32_bf16 v[16:19], v[168:171], v[224:227], v[16:19]
	v_mfma_f32_16x16x32_bf16 v[8:11], v[178:181], v[224:227], v[8:11]
	s_setprio 0
	s_barrier
	v_readfirstlane_b32 s5, v159
	v_lshl_add_u64 v[164:165], v[244:245], 0, s[48:49]
	s_mov_b32 m0, s5
	v_readfirstlane_b32 s5, v160
	global_load_lds_dwordx4 v[164:165], off
	v_lshl_add_u64 v[164:165], v[246:247], 0, s[48:49]
	s_mov_b32 m0, s5
	s_nop 0
	global_load_lds_dwordx4 v[164:165], off
	s_waitcnt vmcnt(6)
	s_barrier
	s_setprio 1
	v_mfma_f32_16x16x32_bf16 v[44:47], v[228:231], v[182:185], v[44:47]
	v_mfma_f32_16x16x32_bf16 v[36:39], v[236:239], v[182:185], v[36:39]
	v_mfma_f32_16x16x32_bf16 v[28:31], v[228:231], v[200:203], v[28:31]
	v_mfma_f32_16x16x32_bf16 v[20:23], v[236:239], v[200:203], v[20:23]
	v_mfma_f32_16x16x32_bf16 v[12:15], v[228:231], v[212:215], v[12:15]
	v_mfma_f32_16x16x32_bf16 v[4:7], v[236:239], v[212:215], v[4:7]
	v_mfma_f32_16x16x32_bf16 v[0:3], v[228:231], v[220:223], v[0:3]
	v_mfma_f32_16x16x32_bf16 v[68:71], v[236:239], v[220:223], v[68:71]
	v_mfma_f32_16x16x32_bf16 v[44:47], v[232:235], v[196:199], v[44:47]
	v_mfma_f32_16x16x32_bf16 v[36:39], v[240:243], v[196:199], v[36:39]
	v_mfma_f32_16x16x32_bf16 v[28:31], v[232:235], v[208:211], v[28:31]
	v_mfma_f32_16x16x32_bf16 v[20:23], v[240:243], v[208:211], v[20:23]
	v_mfma_f32_16x16x32_bf16 v[12:15], v[232:235], v[216:219], v[12:15]
	v_mfma_f32_16x16x32_bf16 v[4:7], v[240:243], v[216:219], v[4:7]
	v_mfma_f32_16x16x32_bf16 v[0:3], v[232:235], v[224:227], v[0:3]
	v_mfma_f32_16x16x32_bf16 v[68:71], v[240:243], v[224:227], v[68:71]
	s_setprio 0
	s_add_i32 s1, s1, 2
	s_add_u32 s8, s8, 0x100
	s_addc_u32 s9, s9, 0
	s_cmp_gt_u32 s1, 11
	s_barrier
	s_cbranch_scc0 .LBB0_233
	s_add_u32 s6, s6, 0x40780
	s_addc_u32 s7, s7, 0
	v_readfirstlane_b32 s1, v161
	v_lshl_add_u64 v[128:129], v[128:129], 1, s[6:7]
	s_mov_b32 m0, s1
	v_readfirstlane_b32 s1, v162
	ds_read_b128 v[132:135], v143
	ds_read_b128 v[136:139], v143 offset:1024
	ds_read_b128 v[150:153], v143 offset:2048
	ds_read_b128 v[154:157], v143 offset:3072
	ds_read_b128 v[164:167], v141
	ds_read_b128 v[168:171], v141 offset:1024
	ds_read_b128 v[172:175], v141 offset:2048
	ds_read_b128 v[178:181], v141 offset:3072
	ds_read_b128 v[182:185], v141 offset:4096
	ds_read_b128 v[196:199], v141 offset:5120
	ds_read_b128 v[200:203], v141 offset:6144
	ds_read_b128 v[208:211], v141 offset:7168
	global_load_lds_dwordx4 v[128:129], off
	v_lshl_add_u64 v[128:129], v[130:131], 1, s[6:7]
	s_mov_b32 m0, s1
	s_nop 0
	global_load_lds_dwordx4 v[128:129], off
	s_min_i32 s100, s3, 0x15f
	s_cmpk_lt_i32 s100, 0x140
	s_cbranch_scc0 .Lip_partial
	s_lshr_b32 s101, s100, 5
	s_and_b32 s101, s101, 1
	s_lshr_b32 vcc_lo, s100, 3
	s_and_b32 vcc_lo, vcc_lo, 3
	s_lshl_b32 vcc_hi, s101, 1
	s_add_u32 vcc_lo, vcc_lo, vcc_hi
	s_and_b32 vcc_lo, vcc_lo, 3
	s_lshr_b32 vcc_hi, s100, 6
	s_lshl_b32 vcc_hi, vcc_hi, 2
	s_or_b32 vcc_lo, vcc_lo, vcc_hi
	s_lshl_b32 s101, s101, 3
	s_and_b32 s100, s100, 7
	s_or_b32 s100, s100, s101
	s_branch .Lip_have
.Lip_partial:
	s_sub_u32 s100, s100, 0x140
	s_lshr_b32 vcc_lo, s100, 4
	s_add_u32 vcc_lo, vcc_lo, 20
	s_and_b32 s100, s100, 15
.Lip_have:
	s_or_b32 s100, s100, s92
	s_lshl_b32 s100, s100, 19
	s_lshl_b32 vcc_lo, vcc_lo, 19
	s_add_u32 vcc_lo, vcc_lo, 0x200000
	v_lshrrev_b32_e32 v251, 1, v207
	v_lshlrev_b32_e32 v251, 11, v251
	v_and_b32_e32 v252, 1, v207
	v_lshl_or_b32 v251, v252, 7, v251
	v_add_u32_e32 v252, vcc_lo, v251
	v_add_u32_e32 v251, s100, v251
	global_load_dword v255, v251, s[56:57]
	global_load_dword v255, v252, s[84:85]
	s_barrier
	s_waitcnt lgkmcnt(0)
	s_setprio 1
	s_waitcnt lgkmcnt(0)
	v_mfma_f32_16x16x32_bf16 v[124:127], v[132:135], v[164:167], v[124:127]
	v_mfma_f32_16x16x32_bf16 v[120:123], v[150:153], v[164:167], v[120:123]
	v_mfma_f32_16x16x32_bf16 v[104:107], v[132:135], v[182:185], v[104:107]
	v_mfma_f32_16x16x32_bf16 v[88:91], v[132:135], v[200:203], v[88:91]
	v_mfma_f32_16x16x32_bf16 v[80:83], v[150:153], v[200:203], v[80:83]
	v_mfma_f32_16x16x32_bf16 v[124:127], v[136:139], v[168:171], v[124:127]
	v_mfma_f32_16x16x32_bf16 v[120:123], v[154:157], v[168:171], v[120:123]
	v_mfma_f32_16x16x32_bf16 v[116:119], v[132:135], v[172:175], v[116:119]
	v_mfma_f32_16x16x32_bf16 v[112:115], v[150:153], v[172:175], v[112:115]
	v_mfma_f32_16x16x32_bf16 v[104:107], v[136:139], v[196:199], v[104:107]
	v_mfma_f32_16x16x32_bf16 v[96:99], v[150:153], v[182:185], v[96:99]
	v_mfma_f32_16x16x32_bf16 v[88:91], v[136:139], v[208:211], v[88:91]
	v_mfma_f32_16x16x32_bf16 v[80:83], v[154:157], v[208:211], v[80:83]
	v_mfma_f32_16x16x32_bf16 v[128:131], v[136:139], v[178:181], v[116:119]
	v_mfma_f32_16x16x32_bf16 v[158:161], v[154:157], v[178:181], v[112:115]
	v_mfma_f32_16x16x32_bf16 v[212:215], v[154:157], v[196:199], v[96:99]
	s_setprio 0
	s_barrier
; #define STA(b, h, kt) do { _Pragma("unroll") for (int i_ = 0; i_ < 2; ++i_) __builtin_amdgcn_global_load_lds((const unsigned*)(((kt) < ks ? ab : ab2) + (h) * ah + (kt) * 64 + aoff[i_]), (LAS unsigned*)(lds + ((b) * 2 + (h)) * 16384 + wid * 1024 + i_ * 8192), 16, 0, 0); } while (0)
; #define LDA_(dst, b, h) do { _Pragma("unroll") for (int m_ = 0; m_ < 4; ++m_) _Pragma("unroll") for (int k_ = 0; k_ < 2; ++k_) dst[m_][k_] = *(const bf16x8*)(la + ((b) * 2 + (h)) * 16384 + (m_ * 2 + k_) * 1024); } while (0)
; #define LDB_(dst, b, h) do { _Pragma("unroll") for (int n_ = 0; n_ < 2; ++n_) _Pragma("unroll") for (int k_ = 0; k_ < 2; ++k_) dst[n_][k_] = *(const bf16x8*)(lb + ((b) * 2 + (h)) * 16384 + (n_ * 2 + k_) * 1024); } while (0)
; #define MMA_(ai, bj, Bx) do { __builtin_amdgcn_s_setprio(1); _Pragma("unroll") for (int m_ = 0; m_ < 4; ++m_) _Pragma("unroll") for (int n_ = 0; n_ < 2; ++n_) _Pragma("unroll") for (int k_ = 0; k_ < 2; ++k_) \
;     acc[(ai) * 4 + m_][(bj) * 2 + n_] = MFMA16(Bx[n_][k_], At[m_][k_], acc[(ai) * 4 + m_][(bj) * 2 + n_]); __builtin_amdgcn_s_setprio(0); } while (0)
; #define WAIT_V(n) asm volatile("s_waitcnt vmcnt(" #n ")" ::: "memory")
; #define WAIT_L(n) asm volatile("s_waitcnt lgkmcnt(" #n ")" ::: "memory")
; #define BAR __builtin_amdgcn_s_barrier()
; template <bool ZERO, class Mid>
; DI void gemm_core(const GemmArgs& g, int m0, int n0, char* lds, f32x4 (&acc)[8][4], const Mid& mid) {
;     ...
;   { LDB_(B0, 0, 0); LDA_(At, 0, 0); STA(1, 1, nt - 1);
;     BAR; WAIT_L(0); MMA_(0, 0, B0); BAR;
;     LDB_(B1, 0, 1); BAR; WAIT_L(0); MMA_(0, 1, B1); BAR;
;     LDA_(At, 0, 1); WAIT_V(4); BAR; WAIT_L(0); MMA_(1, 0, B0); MMA_(1, 1, B1); BAR; }
;   { LDB_(B0, 1, 0); LDA_(At, 1, 0); WAIT_V(2); BAR; WAIT_L(0); MMA_(0, 0, B0); BAR;
	s_nop 0
	ds_read_b128 v[96:99], v143 offset:16384
	ds_read_b128 v[112:115], v143 offset:17408
	ds_read_b128 v[116:119], v143 offset:18432
	ds_read_b128 v[216:219], v143 offset:19456
	s_barrier
	s_waitcnt lgkmcnt(0)
	s_setprio 1
	s_waitcnt lgkmcnt(0)
	v_mfma_f32_16x16x32_bf16 v[108:111], v[96:99], v[164:167], v[108:111]
	v_mfma_f32_16x16x32_bf16 v[92:95], v[96:99], v[172:175], v[92:95]
	v_mfma_f32_16x16x32_bf16 v[84:87], v[116:119], v[172:175], v[84:87]
	v_mfma_f32_16x16x32_bf16 v[76:79], v[96:99], v[182:185], v[76:79]
	v_mfma_f32_16x16x32_bf16 v[72:75], v[116:119], v[182:185], v[72:75]
	v_mfma_f32_16x16x32_bf16 v[60:63], v[116:119], v[200:203], v[60:63]
	v_mfma_f32_16x16x32_bf16 v[108:111], v[112:115], v[168:171], v[108:111]
	v_mfma_f32_16x16x32_bf16 v[100:103], v[116:119], v[164:167], v[100:103]
	v_mfma_f32_16x16x32_bf16 v[92:95], v[112:115], v[178:181], v[92:95]
	v_mfma_f32_16x16x32_bf16 v[84:87], v[216:219], v[178:181], v[84:87]
	v_mfma_f32_16x16x32_bf16 v[76:79], v[112:115], v[196:199], v[76:79]
	v_mfma_f32_16x16x32_bf16 v[72:75], v[216:219], v[196:199], v[72:75]
	v_mfma_f32_16x16x32_bf16 v[64:67], v[96:99], v[200:203], v[64:67]
	v_mfma_f32_16x16x32_bf16 v[60:63], v[216:219], v[208:211], v[60:63]
	v_mfma_f32_16x16x32_bf16 v[162:165], v[216:219], v[168:171], v[100:103]
	v_mfma_f32_16x16x32_bf16 v[166:169], v[112:115], v[208:211], v[64:67]
	s_setprio 0
	s_barrier
	s_nop 2
	ds_read_b128 v[64:67], v141 offset:16384
	ds_read_b128 v[100:103], v141 offset:17408
	ds_read_b128 v[170:173], v141 offset:18432
	ds_read_b128 v[178:181], v141 offset:19456
	ds_read_b128 v[182:185], v141 offset:20480
	ds_read_b128 v[196:199], v141 offset:21504
	ds_read_b128 v[200:203], v141 offset:22528
	ds_read_b128 v[208:211], v141 offset:23552
	s_waitcnt vmcnt(6)
	s_barrier
	s_waitcnt lgkmcnt(0)
	s_setprio 1
	s_waitcnt lgkmcnt(0)
	v_mfma_f32_16x16x32_bf16 v[52:55], v[150:153], v[64:67], v[52:55]
	v_mfma_f32_16x16x32_bf16 v[48:51], v[132:135], v[170:173], v[48:51]
	v_mfma_f32_16x16x32_bf16 v[24:27], v[150:153], v[182:185], v[24:27]
	v_mfma_f32_16x16x32_bf16 v[8:11], v[150:153], v[200:203], v[8:11]
	v_mfma_f32_16x16x32_bf16 v[56:59], v[132:135], v[64:67], v[56:59]
	v_mfma_f32_16x16x32_bf16 v[52:55], v[154:157], v[100:103], v[52:55]
	v_mfma_f32_16x16x32_bf16 v[48:51], v[136:139], v[178:181], v[48:51]
	v_mfma_f32_16x16x32_bf16 v[40:43], v[150:153], v[170:173], v[40:43]
	v_mfma_f32_16x16x32_bf16 v[32:35], v[132:135], v[182:185], v[32:35]
	v_mfma_f32_16x16x32_bf16 v[24:27], v[154:157], v[196:199], v[24:27]
	v_mfma_f32_16x16x32_bf16 v[16:19], v[132:135], v[200:203], v[16:19]
	v_mfma_f32_16x16x32_bf16 v[8:11], v[154:157], v[208:211], v[8:11]
	v_mfma_f32_16x16x32_bf16 v[220:223], v[136:139], v[100:103], v[56:59]
	v_mfma_f32_16x16x32_bf16 v[224:227], v[154:157], v[178:181], v[40:43]
	v_mfma_f32_16x16x32_bf16 v[228:231], v[136:139], v[196:199], v[32:35]
	v_mfma_f32_16x16x32_bf16 v[132:135], v[136:139], v[208:211], v[16:19]
	s_setprio 0
	s_setprio 1
	v_mfma_f32_16x16x32_bf16 v[16:19], v[96:99], v[64:67], v[44:47]
	v_mfma_f32_16x16x32_bf16 v[136:139], v[112:115], v[100:103], v[16:19]
	v_mfma_f32_16x16x32_bf16 v[16:19], v[116:119], v[64:67], v[36:39]
	v_mfma_f32_16x16x32_bf16 v[150:153], v[216:219], v[100:103], v[16:19]
	v_mfma_f32_16x16x32_bf16 v[16:19], v[96:99], v[170:173], v[28:31]
	v_mfma_f32_16x16x32_bf16 v[28:31], v[112:115], v[178:181], v[16:19]
	v_mfma_f32_16x16x32_bf16 v[16:19], v[116:119], v[170:173], v[20:23]
	v_mfma_f32_16x16x32_bf16 v[12:15], v[96:99], v[182:185], v[12:15]
	v_mfma_f32_16x16x32_bf16 v[0:3], v[96:99], v[200:203], v[0:3]
	v_mfma_f32_16x16x32_bf16 v[154:157], v[216:219], v[178:181], v[16:19]
	v_mfma_f32_16x16x32_bf16 v[12:15], v[112:115], v[196:199], v[12:15]
	v_mfma_f32_16x16x32_bf16 v[4:7], v[116:119], v[182:185], v[4:7]
	v_mfma_f32_16x16x32_bf16 v[178:181], v[112:115], v[208:211], v[0:3]
	v_mfma_f32_16x16x32_bf16 v[0:3], v[116:119], v[200:203], v[68:71]
	v_mfma_f32_16x16x32_bf16 v[170:173], v[216:219], v[196:199], v[4:7]
	v_mfma_f32_16x16x32_bf16 v[182:185], v[216:219], v[208:211], v[0:3]
	s_setprio 0
	s_barrier
	s_nop 3
	ds_read_b128 v[0:3], v143 offset:32768
	ds_read_b128 v[4:7], v143 offset:33792
	ds_read_b128 v[196:199], v143 offset:34816
	ds_read_b128 v[200:203], v143 offset:35840
	ds_read_b128 v[16:19], v141 offset:32768
	ds_read_b128 v[20:23], v141 offset:33792
	ds_read_b128 v[40:43], v141 offset:34816
	ds_read_b128 v[44:47], v141 offset:35840
	ds_read_b128 v[56:59], v141 offset:36864
	ds_read_b128 v[208:211], v141 offset:37888
	ds_read_b128 v[216:219], v141 offset:38912
	ds_read_b128 v[232:235], v141 offset:39936
	s_waitcnt vmcnt(4)
	s_barrier
; #define LDA_(dst, b, h) do { _Pragma("unroll") for (int m_ = 0; m_ < 4; ++m_) _Pragma("unroll") for (int k_ = 0; k_ < 2; ++k_) dst[m_][k_] = *(const bf16x8*)(la + ((b) * 2 + (h)) * 16384 + (m_ * 2 + k_) * 1024); } while (0)
; #define LDB_(dst, b, h) do { _Pragma("unroll") for (int n_ = 0; n_ < 2; ++n_) _Pragma("unroll") for (int k_ = 0; k_ < 2; ++k_) dst[n_][k_] = *(const bf16x8*)(lb + ((b) * 2 + (h)) * 16384 + (n_ * 2 + k_) * 1024); } while (0)
; #define MMA_(ai, bj, Bx) do { __builtin_amdgcn_s_setprio(1); _Pragma("unroll") for (int m_ = 0; m_ < 4; ++m_) _Pragma("unroll") for (int n_ = 0; n_ < 2; ++n_) _Pragma("unroll") for (int k_ = 0; k_ < 2; ++k_) \
;     acc[(ai) * 4 + m_][(bj) * 2 + n_] = MFMA16(Bx[n_][k_], At[m_][k_], acc[(ai) * 4 + m_][(bj) * 2 + n_]); __builtin_amdgcn_s_setprio(0); } while (0)
; #define WAIT_V(n) asm volatile("s_waitcnt vmcnt(" #n ")" ::: "memory")
; #define WAIT_L(n) asm volatile("s_waitcnt lgkmcnt(" #n ")" ::: "memory")
; #define BAR __builtin_amdgcn_s_barrier()
; template <bool ZERO, class Mid>
; DI void gemm_core(const GemmArgs& g, int m0, int n0, char* lds, f32x4 (&acc)[8][4], const Mid& mid) {
;     ...
;     LDA_(At, 0, 1); WAIT_V(4); BAR; WAIT_L(0); MMA_(1, 0, B0); MMA_(1, 1, B1); BAR; }
;   { LDB_(B0, 1, 0); LDA_(At, 1, 0); WAIT_V(2); BAR; WAIT_L(0); MMA_(0, 0, B0); BAR;
;     LDB_(B1, 1, 1); WAIT_V(0); BAR; WAIT_L(0); MMA_(0, 1, B1); BAR;
;     LDA_(At, 1, 1); BAR; WAIT_L(0); MMA_(1, 0, B0); MMA_(1, 1, B1); BAR; }
;   if (wr == 0) BAR;
	s_waitcnt lgkmcnt(0)
	s_setprio 1
	s_waitcnt lgkmcnt(0)
	v_mfma_f32_16x16x32_bf16 v[32:35], v[0:3], v[16:19], v[124:127]
	v_mfma_f32_16x16x32_bf16 v[112:115], v[4:7], v[20:23], v[32:35]
	v_mfma_f32_16x16x32_bf16 v[32:35], v[196:199], v[16:19], v[120:123]
	v_mfma_f32_16x16x32_bf16 v[116:119], v[200:203], v[20:23], v[32:35]
	v_mfma_f32_16x16x32_bf16 v[32:35], v[0:3], v[40:43], v[128:131]
	v_mfma_f32_16x16x32_bf16 v[96:99], v[4:7], v[44:47], v[32:35]
	v_mfma_f32_16x16x32_bf16 v[32:35], v[196:199], v[40:43], v[158:161]
	v_mfma_f32_16x16x32_bf16 v[100:103], v[200:203], v[44:47], v[32:35]
	v_mfma_f32_16x16x32_bf16 v[32:35], v[0:3], v[56:59], v[104:107]
	v_mfma_f32_16x16x32_bf16 v[64:67], v[4:7], v[208:211], v[32:35]
	v_mfma_f32_16x16x32_bf16 v[32:35], v[196:199], v[56:59], v[212:215]
	v_mfma_f32_16x16x32_bf16 v[68:71], v[200:203], v[208:211], v[32:35]
	v_mfma_f32_16x16x32_bf16 v[32:35], v[0:3], v[216:219], v[88:91]
	v_mfma_f32_16x16x32_bf16 v[36:39], v[196:199], v[216:219], v[80:83]
	v_mfma_f32_16x16x32_bf16 v[32:35], v[4:7], v[232:235], v[32:35]
	v_mfma_f32_16x16x32_bf16 v[36:39], v[200:203], v[232:235], v[36:39]
	s_setprio 0
	s_barrier
	ds_read_b128 v[128:131], v143 offset:49152
	ds_read_b128 v[158:161], v143 offset:50176
	ds_read_b128 v[212:215], v143 offset:51200
	ds_read_b128 v[236:239], v143 offset:52224
	s_waitcnt vmcnt(2)
	s_barrier
	s_waitcnt lgkmcnt(0)
	s_setprio 1
	s_waitcnt lgkmcnt(0)
	v_mfma_f32_16x16x32_bf16 v[80:83], v[128:131], v[16:19], v[108:111]
	v_mfma_f32_16x16x32_bf16 v[16:19], v[212:215], v[16:19], v[162:165]
	v_mfma_f32_16x16x32_bf16 v[124:127], v[236:239], v[20:23], v[16:19]
	v_mfma_f32_16x16x32_bf16 v[16:19], v[128:131], v[40:43], v[92:95]
	v_mfma_f32_16x16x32_bf16 v[104:107], v[158:161], v[44:47], v[16:19]
	v_mfma_f32_16x16x32_bf16 v[16:19], v[212:215], v[40:43], v[84:87]
	v_mfma_f32_16x16x32_bf16 v[108:111], v[236:239], v[44:47], v[16:19]
	v_mfma_f32_16x16x32_bf16 v[16:19], v[128:131], v[56:59], v[76:79]
	v_mfma_f32_16x16x32_bf16 v[88:91], v[158:161], v[208:211], v[16:19]
	v_mfma_f32_16x16x32_bf16 v[16:19], v[212:215], v[56:59], v[72:75]
	v_mfma_f32_16x16x32_bf16 v[92:95], v[236:239], v[208:211], v[16:19]
	v_mfma_f32_16x16x32_bf16 v[16:19], v[128:131], v[216:219], v[166:169]
	v_mfma_f32_16x16x32_bf16 v[56:59], v[158:161], v[232:235], v[16:19]
	v_mfma_f32_16x16x32_bf16 v[16:19], v[212:215], v[216:219], v[60:63]
	v_mfma_f32_16x16x32_bf16 v[120:123], v[158:161], v[20:23], v[80:83]
	v_mfma_f32_16x16x32_bf16 v[60:63], v[236:239], v[232:235], v[16:19]
	s_setprio 0
	s_barrier
	ds_read_b128 v[84:87], v141 offset:49152
	ds_read_b128 v[162:165], v141 offset:50176
	ds_read_b128 v[166:169], v141 offset:51200
	ds_read_b128 v[208:211], v141 offset:52224
	ds_read_b128 v[216:219], v141 offset:53248
	ds_read_b128 v[232:235], v141 offset:54272
	ds_read_b128 v[240:243], v141 offset:55296
	ds_read_b128 v[244:247], v141 offset:56320
	s_barrier
	s_waitcnt lgkmcnt(0)
	s_setprio 1
	s_waitcnt lgkmcnt(0)
	v_mfma_f32_16x16x32_bf16 v[16:19], v[0:3], v[84:87], v[220:223]
	v_mfma_f32_16x16x32_bf16 v[72:75], v[4:7], v[162:165], v[16:19]
	v_mfma_f32_16x16x32_bf16 v[16:19], v[196:199], v[84:87], v[52:55]
	v_mfma_f32_16x16x32_bf16 v[76:79], v[200:203], v[162:165], v[16:19]
	v_mfma_f32_16x16x32_bf16 v[16:19], v[0:3], v[166:169], v[48:51]
	v_mfma_f32_16x16x32_bf16 v[40:43], v[4:7], v[208:211], v[16:19]
	v_mfma_f32_16x16x32_bf16 v[16:19], v[196:199], v[166:169], v[224:227]
	v_mfma_f32_16x16x32_bf16 v[44:47], v[200:203], v[208:211], v[16:19]
	v_mfma_f32_16x16x32_bf16 v[16:19], v[0:3], v[216:219], v[228:231]
	v_mfma_f32_16x16x32_bf16 v[0:3], v[0:3], v[240:243], v[132:135]
	v_mfma_f32_16x16x32_bf16 v[16:19], v[4:7], v[232:235], v[16:19]
	v_mfma_f32_16x16x32_bf16 v[20:23], v[196:199], v[216:219], v[24:27]
	v_mfma_f32_16x16x32_bf16 v[0:3], v[4:7], v[244:247], v[0:3]
	v_mfma_f32_16x16x32_bf16 v[4:7], v[196:199], v[240:243], v[8:11]
	v_mfma_f32_16x16x32_bf16 v[20:23], v[200:203], v[232:235], v[20:23]
	v_mfma_f32_16x16x32_bf16 v[4:7], v[200:203], v[244:247], v[4:7]
	s_setprio 0
	s_setprio 1
	v_mfma_f32_16x16x32_bf16 v[8:11], v[128:131], v[84:87], v[136:139]
	v_mfma_f32_16x16x32_bf16 v[80:83], v[158:161], v[162:165], v[8:11]
	v_mfma_f32_16x16x32_bf16 v[8:11], v[212:215], v[84:87], v[150:153]
	v_mfma_f32_16x16x32_bf16 v[84:87], v[236:239], v[162:165], v[8:11]
	v_mfma_f32_16x16x32_bf16 v[8:11], v[128:131], v[166:169], v[28:31]
	v_mfma_f32_16x16x32_bf16 v[48:51], v[158:161], v[208:211], v[8:11]
	v_mfma_f32_16x16x32_bf16 v[8:11], v[212:215], v[166:169], v[154:157]
	v_mfma_f32_16x16x32_bf16 v[52:55], v[236:239], v[208:211], v[8:11]
	v_mfma_f32_16x16x32_bf16 v[8:11], v[128:131], v[216:219], v[12:15]
	v_mfma_f32_16x16x32_bf16 v[24:27], v[158:161], v[232:235], v[8:11]
	v_mfma_f32_16x16x32_bf16 v[8:11], v[212:215], v[216:219], v[170:173]
	v_mfma_f32_16x16x32_bf16 v[28:31], v[236:239], v[232:235], v[8:11]
	v_mfma_f32_16x16x32_bf16 v[8:11], v[128:131], v[240:243], v[178:181]
	v_mfma_f32_16x16x32_bf16 v[12:15], v[212:215], v[240:243], v[182:185]
	v_mfma_f32_16x16x32_bf16 v[8:11], v[158:161], v[244:247], v[8:11]
	v_mfma_f32_16x16x32_bf16 v[12:15], v[236:239], v[244:247], v[12:15]
	s_setprio 0
	s_movk_i32 s1, 0x100
	v_cmp_gt_u32_e32 vcc, s1, v140
	s_barrier
	s_and_saveexec_b64 s[6:7], vcc
	s_cbranch_execz .LBB0_236
	s_barrier

; __global__ void __launch_bounds__(NTB, 2) fwd(Params p) {
	.amdhsa_kernel _Z3fwd6Params
		.amdhsa_group_segment_fixed_size 0
		.amdhsa_private_segment_fixed_size 0
		.amdhsa_kernarg_size 456
		.amdhsa_user_sgpr_count 2
		.amdhsa_user_sgpr_dispatch_ptr 0
		.amdhsa_user_sgpr_queue_ptr 0
		.amdhsa_user_sgpr_kernarg_segment_ptr 1
		.amdhsa_user_sgpr_dispatch_id 0
		.amdhsa_user_sgpr_kernarg_preload_length 0
		.amdhsa_user_sgpr_kernarg_preload_offset 0
		.amdhsa_user_sgpr_private_segment_size 0
		.amdhsa_uses_dynamic_stack 0
		.amdhsa_enable_private_segment 0
		.amdhsa_system_sgpr_workgroup_id_x 1
		.amdhsa_system_sgpr_workgroup_id_y 0
		.amdhsa_system_sgpr_workgroup_id_z 0
		.amdhsa_system_sgpr_workgroup_info 0
		.amdhsa_system_vgpr_workitem_id 2
		.amdhsa_next_free_vgpr 256
		.amdhsa_next_free_sgpr 102
		.amdhsa_accum_offset 256
		.amdhsa_reserve_vcc 1
		.amdhsa_float_round_mode_32 0
		.amdhsa_float_round_mode_16_64 0
		.amdhsa_float_denorm_mode_32 3
		.amdhsa_float_denorm_mode_16_64 3
		.amdhsa_dx10_clamp 1
		.amdhsa_ieee_mode 1
		.amdhsa_fp16_overflow 0
		.amdhsa_tg_split 0
		.amdhsa_exception_fp_ieee_invalid_op 0
		.amdhsa_exception_fp_denorm_src 0
		.amdhsa_exception_fp_ieee_div_zero 0
		.amdhsa_exception_fp_ieee_overflow 0
		.amdhsa_exception_fp_ieee_underflow 0
		.amdhsa_exception_fp_ieee_inexact 0
		.amdhsa_exception_int_div_zero 0
	.end_amdhsa_kernel

; __global__ void __launch_bounds__(NTB, 2) fwd(Params p) {
amdhsa.kernels:
  - .agpr_count:     0
    .args:
      - .offset:         0
        .size:           200
        .value_kind:     by_value
      - .offset:         200
        .size:           4
        .value_kind:     hidden_block_count_x
      - .offset:         204
        .size:           4
        .value_kind:     hidden_block_count_y
      - .offset:         208
        .size:           4
        .value_kind:     hidden_block_count_z
      - .offset:         212
        .size:           2
        .value_kind:     hidden_group_size_x
      - .offset:         214
        .size:           2
        .value_kind:     hidden_group_size_y
      - .offset:         216
        .size:           2
        .value_kind:     hidden_group_size_z
      - .offset:         218
        .size:           2
        .value_kind:     hidden_remainder_x
      - .offset:         220
        .size:           2
        .value_kind:     hidden_remainder_y
      - .offset:         222
        .size:           2
        .value_kind:     hidden_remainder_z
      - .offset:         240
        .size:           8
        .value_kind:     hidden_global_offset_x
      - .offset:         248
        .size:           8
        .value_kind:     hidden_global_offset_y
      - .offset:         256
        .size:           8
        .value_kind:     hidden_global_offset_z
      - .offset:         264
        .size:           2
        .value_kind:     hidden_grid_dims
      - .offset:         288
        .size:           8
        .value_kind:     hidden_multigrid_sync_arg
      - .offset:         320
        .size:           4
        .value_kind:     hidden_dynamic_lds_size
    .group_segment_fixed_size: 0
    .kernarg_segment_align: 8
    .kernarg_segment_size: 456
    .language:       OpenCL C
    .language_version:
      - 2
      - 0
    .max_flat_workgroup_size: 512
    .name:           _Z3fwd6Params
    .private_segment_fixed_size: 0
    .sgpr_count:     108
    .sgpr_spill_count: 12
    .symbol:         _Z3fwd6Params.kd
    .uniform_work_group_size: 1
    .uses_dynamic_stack: false
    .vgpr_count:     256
    .vgpr_spill_count: 0
    .wavefront_size: 64
